# baseline (speedup 1.0000x reference)
.LBB0_89:
	v_mov_b32_e32 v112, v22
	v_mov_b32_e32 v113, v23
	v_mov_b32_e32 v114, v24
	v_mov_b32_e32 v115, v25
	v_mov_b32_e32 v3, 0
	v_lshlrev_b32_e32 v70, 4, v28
	s_and_saveexec_b64 s[60:61], vcc
	s_cbranch_execz .LBB0_118
	s_mov_b64 s[92:93], s[14:15]
	v_lshl_add_u64 v[22:23], s[12:13], 0, v[2:3]
	s_waitcnt vmcnt(0) lgkmcnt(0)
	v_cndmask_b32_e64 v55, -1, v4, s[0:1]
	s_movk_i32 s0, 0x880
	v_mov_b32_e32 v2, 0x1dd00
	v_mad_u32_u24 v4, v80, s0, v2
	v_lshlrev_b32_e32 v2, 1, v1
	v_mov_b32_e32 v27, v3
	v_mbcnt_hi_u32_b32 v2, -1, v29
	v_lshl_add_u64 v[72:73], v[22:23], 0, v[26:27]
	v_and_b32_e32 v23, 64, v2
	v_xor_b32_e32 v22, 16, v2
	v_add_u32_e32 v23, 64, v23
	v_cmp_lt_i32_e32 vcc, v22, v23
	v_lshlrev_b32_e32 v88, 2, v28
	v_and_b32_e32 v24, 7, v0
	v_cndmask_b32_e32 v22, v2, v22, vcc
	v_lshlrev_b32_e32 v90, 2, v22
	v_xor_b32_e32 v22, 32, v2
	v_cmp_lt_i32_e32 vcc, v22, v23
	s_mov_b32 s24, 0x10000
	v_cndmask_b32_e32 v2, v2, v22, vcc
	v_lshlrev_b32_e32 v91, 2, v2
	v_lshrrev_b32_e32 v2, 2, v79
	v_mul_u32_u24_e32 v22, 0x88, v79
	v_add3_u32 v92, v4, v22, v1
	v_or_b32_e32 v2, v88, v2
	v_lshlrev_b32_e32 v22, 3, v0
	v_mul_u32_u24_e32 v2, 0x88, v2
	v_and_b32_e32 v22, 24, v22
	v_add3_u32 v93, v4, v2, v22
	v_lshlrev_b32_e32 v2, 5, v24
	v_or3_b32 v78, v2, v1, s24
	v_bfe_u32 v2, v0, 1, 2
	v_lshrrev_b32_e32 v89, 3, v79
	v_cmp_eq_u32_e64 s[6:7], 4, v24
	v_cmp_eq_u32_e64 s[8:9], 3, v24
	v_cmp_eq_u32_e64 s[10:11], 2, v24
	v_cmp_eq_u32_e64 s[12:13], 1, v24
	v_cmp_eq_u32_e64 s[14:15], 0, v24
	v_cmp_eq_u32_e64 s[16:17], 7, v24
	v_cmp_eq_u32_e64 s[18:19], 6, v24
	v_cmp_eq_u32_e64 s[20:21], 5, v24
	v_cmp_eq_u32_e64 s[22:23], 0, v2
	v_cmp_eq_u32_e64 s[24:25], 1, v2
	v_cmp_eq_u32_e64 s[26:27], 2, v2
	v_cmp_eq_u32_e64 s[28:29], 3, v2
	s_and_b64 s[22:23], s[22:23], s[4:5]
	s_and_b64 s[24:25], s[24:25], s[4:5]
	s_and_b64 s[26:27], s[26:27], s[4:5]
	s_and_b64 s[28:29], s[28:29], s[4:5]
	v_mov_b32_e32 v71, 0xf149f2ca
	s_mov_b64 s[62:63], 0
	s_mov_b32 s69, 0xf149f2ca
	s_mov_b32 s70, 0xefa18f08
	s_mov_b32 s71, 0x41000000
	s_movk_i32 s72, 0x110
	s_mov_b32 s77, 0x26500
	s_mov_b32 s73, 0x2650c
	s_mov_b32 s80, -1
	s_mov_b32 s81, 0
	s_mov_b32 s82, 0
	s_mov_b32 s83, 0x7fffffff
	s_mov_b64 s[84:85], 0
	v_mov_b32_e32 v100, 0
	v_mov_b32_e32 v4, 0
	v_mov_b32_e32 v103, 0xf149f2ca
	v_mov_b32_e32 v46, v3
	v_mov_b32_e32 v47, v3
	v_mov_b32_e32 v48, v3
	v_mov_b32_e32 v49, v3
	v_mov_b32_e32 v50, v3
	v_mov_b32_e32 v51, v3
	v_mov_b32_e32 v52, v3
	v_mov_b32_e32 v53, v3
	v_mov_b32_e32 v38, v3
	v_mov_b32_e32 v39, v3
	v_mov_b32_e32 v40, v3
	v_mov_b32_e32 v41, v3
	v_mov_b32_e32 v42, v3
	v_mov_b32_e32 v43, v3
	v_mov_b32_e32 v44, v3
	v_mov_b32_e32 v45, v3
	v_mov_b32_e32 v30, v3
	v_mov_b32_e32 v31, v3
	v_mov_b32_e32 v32, v3
	v_mov_b32_e32 v33, v3
	v_mov_b32_e32 v34, v3
	v_mov_b32_e32 v35, v3
	v_mov_b32_e32 v36, v3
	v_mov_b32_e32 v37, v3
	v_mov_b32_e32 v22, v3
	v_mov_b32_e32 v23, v3
	v_mov_b32_e32 v24, v3
	v_mov_b32_e32 v25, v3
	v_mov_b32_e32 v26, v3
	v_mov_b32_e32 v28, v3
	v_mov_b32_e32 v29, v3
	v_readfirstlane_b32 s86, v80
	s_mov_b32 s87, 0
	v_readfirstlane_b32 s88, v99
	v_readfirstlane_b32 s89, v5
	v_readfirstlane_b32 s96, v54
	v_readfirstlane_b32 s97, v84
	v_readfirstlane_b32 s98, v85
	v_readfirstlane_b32 s99, v81
	v_readfirstlane_b32 s100, v83
	s_mov_b32 s101, 0
	v_mov_b32_e32 v84, v82
	s_cmp_ge_i32 s96, s68
	s_cselect_b32 s100, 0, s100
	s_branch .LBB0_95

.Lattn_skip:
	s_cmp_ge_i32 s86, s68
	s_cbranch_scc1 .LBB0_118
	s_mov_b32 s80, s86
	s_mov_b32 s81, s87
	s_mov_b32 s82, s89
	s_mov_b32 s83, s88
	s_mov_b64 s[84:85], s[90:91]
	s_mov_b32 s86, s96
	s_mov_b32 s87, s97
	s_mov_b32 s88, s100
	s_mov_b32 s89, s99
	s_waitcnt vmcnt(4)
	v_cndmask_b32_e64 v55, -1, v98, s[30:31]
	s_cmp_ge_i32 s96, s68
	s_cbranch_scc1 .LBB0_95
	s_add_i32 s97, s97, 1
	s_lshl_b32 s94, s97, 4
	s_cmp_lt_i32 s94, s100
	s_cbranch_scc1 .LBB0_95
	s_mov_b32 s97, 0
	s_waitcnt lgkmcnt(0)
	v_readfirstlane_b32 s96, v84
	s_cmp_lg_u32 s96, 0x7ffffffe
	s_cbranch_scc1 .Lpc_have
	v_mov_b32_e32 v2, 0x26b40
	v_mov_b32_e32 v104, 1
	s_mov_b64 exec, 1
	ds_add_rtn_u32 v104, v2, v104
	s_mov_b64 exec, -1
	s_waitcnt lgkmcnt(0)
	v_readfirstlane_b32 s101, v104
	s_mov_b32 s96, s101
	s_cmp_ge_i32 s101, s68
	s_cbranch_scc1 .Lpc_have
	s_lshl_b32 s94, s101, 2
	s_add_i32 s94, s94, 0x26dd0
	v_mov_b32_e32 v2, s94
	ds_read_b32 v2, v2
	s_waitcnt lgkmcnt(0)
	v_readfirstlane_b32 s96, v2
.Lpc_have:
	s_sub_i32 s94, s68, 24
	s_cmp_ge_i32 s101, s94
	s_cselect_b32 s34, 1, 0
	s_cbranch_scc1 .Lpc_nograb
	v_mov_b32_e32 v2, 0x26b40
	v_mov_b32_e32 v104, 1
	s_mov_b64 exec, 1
	ds_add_rtn_u32 v104, v2, v104
	s_mov_b64 exec, -1
.Lpc_nograb:
	s_cmp_ge_i32 s96, s68
	s_cbranch_scc1 .Lattn_c1inv
	s_lshl_b32 s94, s96, 1
	s_min_i32 s95, s94, s67
	s_lshl_b32 s95, s95, 3
	s_add_i32 s95, s95, 0x26500
	v_mov_b32_e32 v2, s95
	ds_read_b64 v[106:107], v2
	s_or_b32 s95, s94, 1
	s_min_i32 s74, s95, s67
	s_lshl_b32 s74, s74, 3
	s_add_i32 s74, s74, 0x26504
	v_mov_b32_e32 v2, s74
	ds_read_b32 v105, v2
	s_waitcnt lgkmcnt(0)
	v_readfirstlane_b32 s98, v106
	v_readfirstlane_b32 s99, v107
	v_readfirstlane_b32 s100, v105
	s_cmp_lt_i32 s95, s33
	s_cselect_b32 s100, s100, 0
	s_add_i32 s100, s100, s99
	s_branch .Lattn_map

.Lattn_map:
	s_cmp_lg_u32 s34, 0
	s_cbranch_scc1 .Lpc_setnone
	v_readfirstlane_b32 s101, v104
	s_nop 0
	v_mov_b32_e32 v84, s101
	s_cmp_ge_i32 s101, s68
	s_cbranch_scc1 .LBB0_95
	s_lshl_b32 s94, s101, 2
	s_add_i32 s94, s94, 0x26dd0
	v_mov_b32_e32 v2, s94
	ds_read_b32 v84, v2
	s_branch .LBB0_95
.Lpc_setnone:
	v_mov_b32_e32 v84, 0x7ffffffe
	s_branch .LBB0_95
